# all kernarg pointer loads (t0p, bv, out) and the t0 load hoisted to kernel start; no scalar-memory waits left inside phases 1, exp
# baseline (speedup 1.0000x reference)
_Z7na_mainPKDF16_PKhS0_PKfS4_S4_S4_Pf:
	s_lshl_b32 s3, s2, 5
	s_and_b32 s3, s3, 0xe0
	s_ashr_i32 s2, s2, 3
	s_add_i32 s3, s3, s2
	s_ashr_i32 s2, s3, 6
	s_lshl_b32 s3, s3, 5
	s_and_b32 s14, s3, 0x7e0
	v_mov_b32_e32 v1, 0x7c0
	s_load_dwordx8 s[4:11], s[0:1], 0x0
	s_load_dwordx2 s[18:19], s[0:1], 0x20
	s_load_dwordx2 s[28:29], s[0:1], 0x28
	s_load_dwordx2 s[34:35], s[0:1], 0x30
	s_load_dwordx2 s[30:31], s[0:1], 0x38
	v_med3_u32 v1, s14, 32, v1
	v_subrev_u32_e32 v97, 32, v1
	s_ashr_i32 s3, s2, 31
	v_lshlrev_b32_e32 v58, 1, v97
	s_lshl_b64 s[12:13], s[2:3], 12
	v_mov_b32_e32 v59, 0
	v_sub_u32_e32 v60, s14, v97
	v_lshl_add_u64 v[10:11], s[12:13], 0, v[58:59]
	v_lshlrev_b64 v[2:3], 9, v[10:11]
	v_lshl_or_b32 v22, v60, 6, v0
	s_waitcnt lgkmcnt(0)
	s_load_dword s32, s[28:29], 0x0
	v_and_b32_e32 v208, 31, v0
	v_lshlrev_b32_e32 v208, 5, v208
	global_load_dwordx4 v[192:195], v208, s[18:19]
	global_load_dwordx4 v[196:199], v208, s[18:19] offset:16
	v_lshl_add_u64 v[20:21], s[4:5], 0, v[2:3]
	v_ashrrev_i32_e32 v23, 31, v22
	v_lshl_add_u64 v[2:3], v[22:23], 4, v[20:21]
	global_load_dwordx4 v[12:15], v[2:3], off
	v_or_b32_e32 v28, 0x200, v22
	v_ashrrev_i32_e32 v29, 31, v28
	v_lshl_add_u64 v[2:3], v[28:29], 4, v[20:21]
	global_load_dwordx4 v[16:19], v[2:3], off
	v_or_b32_e32 v184, 0x400, v22
	v_ashrrev_i32_e32 v185, 31, v184
	v_lshl_add_u64 v[184:185], v[184:185], 4, v[20:21]
	v_or_b32_e32 v188, 0x600, v22
	v_ashrrev_i32_e32 v189, 31, v188
	v_lshl_add_u64 v[188:189], v[188:189], 4, v[20:21]
	global_load_dwordx4 v[184:187], v[184:185], off
	global_load_dwordx4 v[188:191], v[188:189], off
	v_lshrrev_b32_e32 v99, 6, v0
	v_and_b32_e32 v98, 63, v0
	v_lshlrev_b32_e32 v118, 13, v99
	v_lshl_or_b32 v58, v98, 5, v118
	s_movk_i32 s15, 0x1000
	v_lshl_add_u64 v[24:25], s[6:7], 0, v[58:59]
	v_or_b32_e32 v32, 0x400, v22
	v_or_b32_e32 v62, 0x600, v22
	v_add_co_u32_e32 v64, vcc, s15, v24
	s_mov_b64 s[12:13], 0x1000
	s_mov_b64 s[16:17], 0x1800
	v_lshlrev_b32_e32 v72, 1, v60
	v_lshrrev_b32_e32 v23, 5, v22
	v_and_b32_e32 v34, 32, v22
	v_ashrrev_i32_e32 v33, 31, v32
	v_ashrrev_i32_e32 v63, 31, v62
	v_addc_co_u32_e32 v65, vcc, 0, v25, vcc
	global_load_dwordx4 v[6:9], v58, s[6:7] offset:16
	global_load_dwordx4 v[2:5], v58, s[6:7]
	global_load_dwordx4 v[54:57], v58, s[6:7] offset:2064
	global_load_dwordx4 v[50:53], v58, s[6:7] offset:2048
	v_lshrrev_b32_e32 v58, 6, v22
	v_bfe_u32 v73, v22, 8, 2
	v_lshl_add_u64 v[26:27], v[24:25], 0, s[12:13]
	v_lshl_add_u64 v[24:25], v[24:25], 0, s[16:17]
	v_cmp_ne_u32_e32 vcc, 0, v34
	v_sub_u32_e32 v75, v23, v72
	global_load_dwordx4 v[42:45], v[64:65], off
	global_load_dwordx4 v[46:49], v[26:27], off offset:16
	global_load_dwordx4 v[34:37], v[64:65], off offset:2048
	global_load_dwordx4 v[38:41], v[24:25], off offset:16
	v_mov_b32_e32 v61, 0x60
	v_cndmask_b32_e32 v74, 0, v61, vcc
	v_add_u32_e32 v33, v74, v58
	v_lshlrev_b32_e32 v64, 2, v33
	v_bfe_u32 v96, v0, 4, 1
	v_and_b32_e32 v100, 15, v0
	v_mov_b32_e32 v30, v59
	v_mov_b32_e32 v31, v59
	v_and_b32_e32 v64, 12, v64
	v_mul_u32_u24_e32 v29, 0xc000, v96
	v_bitop3_b32 v64, v64, v100, v73 bitop3:0x36
	v_lshl_or_b32 v64, v64, 4, v29
	v_lshlrev_b32_e32 v63, 1, v75
	v_lshl_add_u32 v33, v33, 8, v64
	v_bfe_u32 v71, v0, 1, 4
	v_and_b32_e32 v70, 32, v0
	v_lshlrev_b32_e32 v1, 3, v0
	v_lshrrev_b32_e32 v58, 1, v75
	v_and_b32_e32 v1, 8, v1
	v_add_lshl_u32 v58, v58, v70, 8
	v_lshlrev_b32_e32 v121, 3, v99
	v_bfe_u32 v101, v0, 4, 2
	v_lshlrev_b32_e32 v102, 2, v101
	v_and_b32_e32 v116, 31, v0
	v_bfe_u32 v119, v0, 5, 1
	v_lshlrev_b32_e32 v124, 1, v119
	v_lshlrev_b32_e32 v117, 8, v116
	v_lshrrev_b32_e32 v95, 4, v0
	s_movk_i32 s16, 0x60
	s_mov_b32 s17, 0xc000
	v_and_b32_e32 v211, 3, v99
	v_lshrrev_b32_e32 v212, 2, v99
	v_lshl_or_b32 v211, v211, 2, v212
	v_xor_b32_e32 v213, v100, v211
	v_mul_u32_u24_e32 v214, 0x60, v119
	v_add3_u32 v214, v214, v60, v99
	v_mul_u32_u24_e32 v215, 0xc000, v96
	v_lshl_add_u32 v214, v214, 8, v215
	v_lshl_or_b32 v220, v213, 4, v214
	v_xor_b32_e32 v221, 32, v220
	v_xor_b32_e32 v216, v71, v211
	v_lshl_add_u32 v217, v119, 5, v99
	v_lshlrev_b32_e32 v217, 8, v217
	v_lshl_or_b32 v216, v216, 4, v217
	v_or_b32_e32 v216, v216, v1
	v_add_u32_e32 v222, 0x23800, v216
	v_xor_b32_e32 v223, 32, v222
	s_waitcnt vmcnt(11)
	ds_write_b128 v220, v[12:15]
	v_fma_mix_f32 v200, v192, v12, 0 op_sel_hi:[0,1,0]
	v_fma_mix_f32 v201, v193, v12, 0 op_sel:[0,1,0] op_sel_hi:[0,1,0]
	v_cvt_f32_f16_e32 v211, v12
	v_cvt_f32_f16_sdwa v212, v12 dst_sel:DWORD dst_unused:UNUSED_PAD src0_sel:WORD_1
	v_fma_mix_f32 v200, v194, v13, v200 op_sel_hi:[0,1,0]
	v_fma_mix_f32 v201, v195, v13, v201 op_sel:[0,1,0] op_sel_hi:[0,1,0]
	v_cvt_f32_f16_e32 v213, v13
	v_cvt_f32_f16_sdwa v214, v13 dst_sel:DWORD dst_unused:UNUSED_PAD src0_sel:WORD_1
	v_fma_mix_f32 v200, v196, v14, v200 op_sel_hi:[0,1,0]
	v_fma_mix_f32 v201, v197, v14, v201 op_sel:[0,1,0] op_sel_hi:[0,1,0]
	v_cvt_f32_f16_e32 v215, v14
	v_cvt_f32_f16_sdwa v216, v14 dst_sel:DWORD dst_unused:UNUSED_PAD src0_sel:WORD_1
	v_fma_mix_f32 v200, v198, v15, v200 op_sel_hi:[0,1,0]
	v_fma_mix_f32 v201, v199, v15, v201 op_sel:[0,1,0] op_sel_hi:[0,1,0]
	v_cvt_f32_f16_e32 v217, v15
	v_cvt_f32_f16_sdwa v218, v15 dst_sel:DWORD dst_unused:UNUSED_PAD src0_sel:WORD_1
	v_cvt_pk_fp8_f32 v224, v211, v212
	v_cvt_pk_fp8_f32 v225, v215, v216
	v_cvt_pk_fp8_f32 v224, v213, v214 op_sel:[0,0,1]
	v_cvt_pk_fp8_f32 v225, v217, v218 op_sel:[0,0,1]
	s_nop 0
	ds_write_b64 v222, v[224:225]
	s_waitcnt vmcnt(10)
	ds_write_b128 v221, v[16:19] offset:2048
	v_fma_mix_f32 v202, v192, v16, 0 op_sel_hi:[0,1,0]
	v_fma_mix_f32 v203, v193, v16, 0 op_sel:[0,1,0] op_sel_hi:[0,1,0]
	v_cvt_f32_f16_e32 v211, v16
	v_cvt_f32_f16_sdwa v212, v16 dst_sel:DWORD dst_unused:UNUSED_PAD src0_sel:WORD_1
	v_fma_mix_f32 v202, v194, v17, v202 op_sel_hi:[0,1,0]
	v_fma_mix_f32 v203, v195, v17, v203 op_sel:[0,1,0] op_sel_hi:[0,1,0]
	v_cvt_f32_f16_e32 v213, v17
	v_cvt_f32_f16_sdwa v214, v17 dst_sel:DWORD dst_unused:UNUSED_PAD src0_sel:WORD_1
	v_fma_mix_f32 v202, v196, v18, v202 op_sel_hi:[0,1,0]
	v_fma_mix_f32 v203, v197, v18, v203 op_sel:[0,1,0] op_sel_hi:[0,1,0]
	v_cvt_f32_f16_e32 v215, v18
	v_cvt_f32_f16_sdwa v216, v18 dst_sel:DWORD dst_unused:UNUSED_PAD src0_sel:WORD_1
	v_fma_mix_f32 v202, v198, v19, v202 op_sel_hi:[0,1,0]
	v_fma_mix_f32 v203, v199, v19, v203 op_sel:[0,1,0] op_sel_hi:[0,1,0]
	v_cvt_f32_f16_e32 v217, v19
	v_cvt_f32_f16_sdwa v218, v19 dst_sel:DWORD dst_unused:UNUSED_PAD src0_sel:WORD_1
	v_cvt_pk_fp8_f32 v226, v211, v212
	v_cvt_pk_fp8_f32 v227, v215, v216
	v_cvt_pk_fp8_f32 v226, v213, v214 op_sel:[0,0,1]
	v_cvt_pk_fp8_f32 v227, v217, v218 op_sel:[0,0,1]
	s_nop 0
	ds_write_b64 v223, v[226:227] offset:2048
	s_waitcnt vmcnt(9)
	ds_write_b128 v220, v[184:187] offset:4096
	v_fma_mix_f32 v204, v192, v184, 0 op_sel_hi:[0,1,0]
	v_fma_mix_f32 v205, v193, v184, 0 op_sel:[0,1,0] op_sel_hi:[0,1,0]
	v_cvt_f32_f16_e32 v211, v184
	v_cvt_f32_f16_sdwa v212, v184 dst_sel:DWORD dst_unused:UNUSED_PAD src0_sel:WORD_1
	v_fma_mix_f32 v204, v194, v185, v204 op_sel_hi:[0,1,0]
	v_fma_mix_f32 v205, v195, v185, v205 op_sel:[0,1,0] op_sel_hi:[0,1,0]
	v_cvt_f32_f16_e32 v213, v185
	v_cvt_f32_f16_sdwa v214, v185 dst_sel:DWORD dst_unused:UNUSED_PAD src0_sel:WORD_1
	v_fma_mix_f32 v204, v196, v186, v204 op_sel_hi:[0,1,0]
	v_fma_mix_f32 v205, v197, v186, v205 op_sel:[0,1,0] op_sel_hi:[0,1,0]
	v_cvt_f32_f16_e32 v215, v186
	v_cvt_f32_f16_sdwa v216, v186 dst_sel:DWORD dst_unused:UNUSED_PAD src0_sel:WORD_1
	v_fma_mix_f32 v204, v198, v187, v204 op_sel_hi:[0,1,0]
	v_fma_mix_f32 v205, v199, v187, v205 op_sel:[0,1,0] op_sel_hi:[0,1,0]
	v_cvt_f32_f16_e32 v217, v187
	v_cvt_f32_f16_sdwa v218, v187 dst_sel:DWORD dst_unused:UNUSED_PAD src0_sel:WORD_1
	v_cvt_pk_fp8_f32 v228, v211, v212
	v_cvt_pk_fp8_f32 v229, v215, v216
	v_cvt_pk_fp8_f32 v228, v213, v214 op_sel:[0,0,1]
	v_cvt_pk_fp8_f32 v229, v217, v218 op_sel:[0,0,1]
	s_nop 0
	ds_write_b64 v222, v[228:229] offset:4096
	s_waitcnt vmcnt(8)
	ds_write_b128 v221, v[188:191] offset:6144
	v_fma_mix_f32 v206, v192, v188, 0 op_sel_hi:[0,1,0]
	v_fma_mix_f32 v207, v193, v188, 0 op_sel:[0,1,0] op_sel_hi:[0,1,0]
	v_cvt_f32_f16_e32 v211, v188
	v_cvt_f32_f16_sdwa v212, v188 dst_sel:DWORD dst_unused:UNUSED_PAD src0_sel:WORD_1
	v_fma_mix_f32 v206, v194, v189, v206 op_sel_hi:[0,1,0]
	v_fma_mix_f32 v207, v195, v189, v207 op_sel:[0,1,0] op_sel_hi:[0,1,0]
	v_cvt_f32_f16_e32 v213, v189
	v_cvt_f32_f16_sdwa v214, v189 dst_sel:DWORD dst_unused:UNUSED_PAD src0_sel:WORD_1
	v_fma_mix_f32 v206, v196, v190, v206 op_sel_hi:[0,1,0]
	v_fma_mix_f32 v207, v197, v190, v207 op_sel:[0,1,0] op_sel_hi:[0,1,0]
	v_cvt_f32_f16_e32 v215, v190
	v_cvt_f32_f16_sdwa v216, v190 dst_sel:DWORD dst_unused:UNUSED_PAD src0_sel:WORD_1
	v_fma_mix_f32 v206, v198, v191, v206 op_sel_hi:[0,1,0]
	v_fma_mix_f32 v207, v199, v191, v207 op_sel:[0,1,0] op_sel_hi:[0,1,0]
	v_cvt_f32_f16_e32 v217, v191
	v_cvt_f32_f16_sdwa v218, v191 dst_sel:DWORD dst_unused:UNUSED_PAD src0_sel:WORD_1
	v_cvt_pk_fp8_f32 v230, v211, v212
	v_cvt_pk_fp8_f32 v231, v215, v216
	v_cvt_pk_fp8_f32 v230, v213, v214 op_sel:[0,0,1]
	v_cvt_pk_fp8_f32 v231, v217, v218 op_sel:[0,0,1]
	s_nop 0
	ds_write_b64 v223, v[230:231] offset:6144
	v_add_f32_e32 v200, v200, v201
	v_add_f32_e32 v202, v202, v203
	v_add_f32_e32 v204, v204, v205
	v_add_f32_e32 v206, v206, v207
	v_lshlrev_b32_e32 v208, 7, v119
	v_lshl_add_u32 v208, v99, 2, v208
	v_add_u32_e32 v208, 0x27800, v208
	v_add_f32_dpp v200, v200, v200 quad_perm:[1,0,3,2] row_mask:0xf bank_mask:0xf
	v_add_f32_dpp v202, v202, v202 quad_perm:[1,0,3,2] row_mask:0xf bank_mask:0xf
	v_add_f32_dpp v204, v204, v204 quad_perm:[1,0,3,2] row_mask:0xf bank_mask:0xf
	v_add_f32_dpp v206, v206, v206 quad_perm:[1,0,3,2] row_mask:0xf bank_mask:0xf
	v_add_f32_dpp v200, v200, v200 quad_perm:[2,3,0,1] row_mask:0xf bank_mask:0xf
	v_add_f32_dpp v202, v202, v202 quad_perm:[2,3,0,1] row_mask:0xf bank_mask:0xf
	v_add_f32_dpp v204, v204, v204 quad_perm:[2,3,0,1] row_mask:0xf bank_mask:0xf
	v_add_f32_dpp v206, v206, v206 quad_perm:[2,3,0,1] row_mask:0xf bank_mask:0xf
	v_add_f32_dpp v200, v200, v200 row_half_mirror row_mask:0xf bank_mask:0xf
	v_add_f32_dpp v202, v202, v202 row_half_mirror row_mask:0xf bank_mask:0xf
	v_add_f32_dpp v204, v204, v204 row_half_mirror row_mask:0xf bank_mask:0xf
	v_add_f32_dpp v206, v206, v206 row_half_mirror row_mask:0xf bank_mask:0xf
	v_add_f32_dpp v200, v200, v200 row_mirror row_mask:0xf bank_mask:0xf
	v_add_f32_dpp v202, v202, v202 row_mirror row_mask:0xf bank_mask:0xf
	v_add_f32_dpp v204, v204, v204 row_mirror row_mask:0xf bank_mask:0xf
	v_add_f32_dpp v206, v206, v206 row_mirror row_mask:0xf bank_mask:0xf
	v_add_f32_dpp v200, v200, v200 row_bcast:15 row_mask:0xa bank_mask:0xf
	v_add_f32_dpp v202, v202, v202 row_bcast:15 row_mask:0xa bank_mask:0xf
	v_add_f32_dpp v204, v204, v204 row_bcast:15 row_mask:0xa bank_mask:0xf
	v_add_f32_dpp v206, v206, v206 row_bcast:15 row_mask:0xa bank_mask:0xf
	s_mov_b32 exec_lo, 0xffff0000
	s_mov_b32 exec_hi, 0xffff0000
	ds_write_b32 v208, v200
	ds_write_b32 v208, v202 offset:32
	ds_write_b32 v208, v204 offset:64
	ds_write_b32 v208, v206 offset:96
	s_mov_b64 exec, -1
	v_lshlrev_b32_e32 v201, 7, v99
	v_lshl_or_b32 v201, v119, 4, v201
	global_load_dwordx4 v[184:187], v201, s[10:11]
	global_load_dwordx4 v[188:191], v201, s[10:11] offset:32
	global_load_dwordx4 v[192:195], v201, s[10:11] offset:64
	global_load_dwordx4 v[196:199], v201, s[10:11] offset:96
	v_cmp_lt_i32_e32 vcc, v121, v60
	s_nop 0
	v_mov_b32_e32 v15, v59
	v_cndmask_b32_e64 v12, 32, 0, vcc
	v_add_u32_e32 v16, v12, v121
	v_or_b32_e32 v12, v16, v101
	v_lshlrev_b32_e32 v58, 1, v12
	v_lshrrev_b32_e32 v12, 5, v0
	v_and_b32_e32 v12, 2, v12
	v_bitop3_b32 v14, v102, v100, v12 bitop3:0x36
	v_lshl_add_u64 v[12:13], v[10:11], 0, v[58:59]
	v_lshlrev_b64 v[12:13], 9, v[12:13]
	v_lshlrev_b32_e32 v16, 8, v16
	v_lshl_add_u64 v[12:13], s[4:5], 0, v[12:13]
	v_lshlrev_b32_e32 v14, 4, v14
	v_readfirstlane_b32 s6, v16
	v_add_u32_e32 v17, 0xc000, v16
	v_lshl_add_u64 v[12:13], v[12:13], 0, v[14:15]
	s_mov_b32 m0, s6
	s_mov_b64 s[6:7], 0x100
	v_readfirstlane_b32 s12, v17
	global_load_lds_dwordx4 v[12:13], off
	v_lshl_add_u64 v[12:13], v[12:13], 0, s[6:7]
	s_mov_b32 m0, s12
	v_or_b32_e32 v58, 1, v58
	global_load_lds_dwordx4 v[12:13], off
	v_lshl_add_u64 v[12:13], v[10:11], 0, v[58:59]
	v_lshlrev_b64 v[12:13], 9, v[12:13]
	v_lshl_add_u64 v[12:13], s[4:5], 0, v[12:13]
	v_lshl_add_u64 v[12:13], v[12:13], 0, v[14:15]
	v_add_u32_e32 v14, 0x6000, v16
	v_bfe_u32 v61, v0, 2, 2
	v_readfirstlane_b32 s12, v14
	v_add_u32_e32 v14, 0x12000, v16
	s_mov_b32 m0, s12
	v_readfirstlane_b32 s12, v14
	global_load_lds_dwordx4 v[12:13], off
	v_lshl_add_u64 v[12:13], v[12:13], 0, s[6:7]
	s_mov_b32 m0, s12
	v_add_u32_e32 v18, 0x23800, v117
	global_load_lds_dwordx4 v[12:13], off
	v_or_b32_e32 v12, 4, v121
	v_cmp_lt_i32_e32 vcc, v12, v60
	s_nop 1
	v_cndmask_b32_e64 v13, 32, 0, vcc
	v_add_u32_e32 v16, v13, v12
	v_or_b32_e32 v13, v16, v101
	v_lshlrev_b32_e32 v58, 1, v13
	v_bfe_u32 v12, v12, 2, 2
	v_bitop3_b32 v14, v102, v100, v12 bitop3:0x36
	v_lshl_add_u64 v[12:13], v[10:11], 0, v[58:59]
	v_lshlrev_b64 v[12:13], 9, v[12:13]
	v_lshlrev_b32_e32 v16, 8, v16
	v_lshl_add_u64 v[12:13], s[4:5], 0, v[12:13]
	v_lshlrev_b32_e32 v14, 4, v14
	v_readfirstlane_b32 s12, v16
	v_add_u32_e32 v17, 0xc000, v16
	v_lshl_add_u64 v[12:13], v[12:13], 0, v[14:15]
	s_mov_b32 m0, s12
	v_readfirstlane_b32 s12, v17
	v_or_b32_e32 v58, 1, v58
	global_load_lds_dwordx4 v[12:13], off
	v_lshl_add_u64 v[12:13], v[12:13], 0, s[6:7]
	s_mov_b32 m0, s12
	v_lshl_add_u64 v[10:11], v[10:11], 0, v[58:59]
	global_load_lds_dwordx4 v[12:13], off
	v_lshlrev_b64 v[10:11], 9, v[10:11]
	v_add_u32_e32 v12, 0x6000, v16
	v_lshl_add_u64 v[10:11], s[4:5], 0, v[10:11]
	v_readfirstlane_b32 s4, v12
	v_add_u32_e32 v12, 0x12000, v16
	v_lshl_add_u64 v[10:11], v[10:11], 0, v[14:15]
	s_mov_b32 m0, s4
	v_readfirstlane_b32 s4, v12
	global_load_lds_dwordx4 v[10:11], off
	v_lshl_add_u64 v[10:11], v[10:11], 0, s[6:7]
	s_mov_b32 m0, s4
	s_nop 0
	global_load_lds_dwordx4 v[10:11], off
	s_waitcnt lgkmcnt(0)
	s_barrier
	v_lshlrev_b32_e32 v10, 2, v0
	v_and_b32_e32 v94, 12, v10
	v_or_b32_e32 v120, v94, v61
	v_bitop3_b32 v10, v124, v94, v61 bitop3:0x1e
	v_lshl_or_b32 v14, v10, 4, v18
	v_bitop3_b32 v10, v124, v120, 1 bitop3:0x36
	v_lshl_or_b32 v19, v10, 4, v18
	ds_read_b128 v[10:13], v14
	ds_read_b128 v[62:65], v14 offset:8192
	ds_read_b128 v[14:17], v19
	ds_read_b128 v[66:69], v19 offset:8192
	v_bitop3_b32 v19, v124, v120, 4 bitop3:0x36
	v_lshl_or_b32 v19, v19, 4, v18
	v_bitop3_b32 v20, v124, v120, 5 bitop3:0x36
	v_lshl_or_b32 v20, v20, 4, v18
	ds_read_b128 v[70:73], v19
	ds_read_b128 v[78:81], v19 offset:8192
	ds_read_b128 v[74:77], v20
	ds_read_b128 v[82:85], v20 offset:8192
	v_bitop3_b32 v19, v124, v120, 8 bitop3:0x36
	v_lshl_or_b32 v19, v19, 4, v18
	v_bitop3_b32 v20, v124, v120, 9 bitop3:0x36
	v_lshl_or_b32 v20, v20, 4, v18
	ds_read_b128 v[86:89], v19
	ds_read_b128 v[104:107], v19 offset:8192
	ds_read_b128 v[90:93], v20
	ds_read_b128 v[108:111], v20 offset:8192
	v_bitop3_b32 v19, v124, v120, 12 bitop3:0x36
	v_lshl_or_b32 v19, v19, 4, v18
	v_bitop3_b32 v20, v124, v120, 13 bitop3:0x36
	v_lshl_or_b32 v18, v20, 4, v18
	ds_read_b128 v[126:129], v19
	ds_read_b128 v[134:137], v19 offset:8192
	ds_read_b128 v[130:133], v18
	ds_read_b128 v[138:141], v18 offset:8192
	v_mov_b32_e32 v103, 0x7f
	v_lshlrev_b32_e32 v58, 7, v99
	v_or_b32_e32 v122, 0x18000, v117
	s_waitcnt vmcnt(18) lgkmcnt(0)
	v_mfma_scale_f32_32x32x64_f8f6f4 v[18:33], v[2:9], v[10:17], 0, v103, v103 op_sel_hi:[0,0,0]
	v_lshlrev_b32_e32 v125, 3, v119
	v_or_b32_e32 v123, 0x1a000, v117
	v_mfma_scale_f32_32x32x64_f8f6f4 v[2:17], v[2:9], v[62:69], 0, v103, v103 op_sel_hi:[0,0,0]
	v_and_b32_e32 v62, 12, v95
	s_waitcnt vmcnt(16)
	v_mfma_scale_f32_32x32x64_f8f6f4 v[18:33], v[50:57], v[70:77], v[18:33], v103, v103 op_sel_hi:[0,0,0]
	v_mfma_scale_f32_32x32x64_f8f6f4 v[2:17], v[50:57], v[78:85], v[2:17], v103, v103 op_sel_hi:[0,0,0]
	s_brev_b32 s10, 60
	v_lshlrev_b32_e32 v58, 6, v0
	v_and_b32_e32 v58, 0x4000, v58
	v_or3_b32 v63, v122, v58, v125
	v_or3_b32 v58, v123, v58, v125
	s_waitcnt vmcnt(14)
	v_mfma_scale_f32_32x32x64_f8f6f4 v[18:33], v[42:49], v[86:93], v[18:33], v103, v103 op_sel_hi:[0,0,0]
	v_mfma_scale_f32_32x32x64_f8f6f4 v[2:17], v[42:49], v[104:111], v[2:17], v103, v103 op_sel_hi:[0,0,0]
	s_nop 0
	s_waitcnt vmcnt(12)
	v_mfma_scale_f32_32x32x64_f8f6f4 v[2:17], v[34:41], v[134:141], v[2:17], v103, v103 op_sel_hi:[0,0,0]
	v_mfma_scale_f32_32x32x64_f8f6f4 v[18:33], v[34:41], v[126:133], v[18:33], v103, v103 op_sel_hi:[0,0,0]
	s_waitcnt vmcnt(8)
	s_nop 15
	s_nop 1
	v_fma_f32 v2, v2, s10, v184
	v_fma_f32 v3, v3, s10, v185
	v_fma_f32 v4, v4, s10, v186
	v_fma_f32 v5, v5, s10, v187
	v_cvt_pk_f16_f32 v2, v2, v3
	v_cvt_pk_f16_f32 v3, v4, v5
	v_bitop3_b32 v4, v95, v120, 12 bitop3:0x6c
	v_pk_fma_f32 v[18:19], v[18:19], s[10:11], v[184:185] op_sel_hi:[1,0,1]
	v_pk_fma_f32 v[20:21], v[20:21], s[10:11], v[186:187] op_sel_hi:[1,0,1]
	v_lshlrev_b32_e32 v4, 4, v4
	v_cvt_pk_f16_f32 v18, v18, v19
	v_cvt_pk_f16_f32 v19, v20, v21
	v_or_b32_e32 v5, v63, v4
	v_or_b32_e32 v4, v58, v4
	ds_write_b64 v5, v[18:19]
	ds_write_b64 v4, v[2:3]
	v_pk_fma_f32 v[2:3], v[22:23], s[10:11], v[188:189] op_sel_hi:[1,0,1]
	v_pk_fma_f32 v[4:5], v[6:7], s[10:11], v[188:189] op_sel_hi:[1,0,1]
	v_pk_fma_f32 v[6:7], v[24:25], s[10:11], v[190:191] op_sel_hi:[1,0,1]
	v_cvt_pk_f16_f32 v2, v2, v3
	v_cvt_pk_f16_f32 v3, v6, v7
	v_pk_fma_f32 v[6:7], v[8:9], s[10:11], v[190:191] op_sel_hi:[1,0,1]
	v_cvt_pk_f16_f32 v4, v4, v5
	v_cvt_pk_f16_f32 v5, v6, v7
	v_bitop3_b32 v6, v62, v120, 1 bitop3:0x36
	v_lshlrev_b32_e32 v6, 4, v6
	v_or_b32_e32 v7, v63, v6
	ds_write_b64 v7, v[2:3]
	v_or_b32_e32 v2, v58, v6
	ds_write_b64 v2, v[4:5]
	v_pk_fma_f32 v[2:3], v[26:27], s[10:11], v[192:193] op_sel_hi:[1,0,1]
	v_pk_fma_f32 v[6:7], v[28:29], s[10:11], v[194:195] op_sel_hi:[1,0,1]
	v_cvt_pk_f16_f32 v2, v2, v3
	v_pk_fma_f32 v[4:5], v[10:11], s[10:11], v[192:193] op_sel_hi:[1,0,1]
	v_cvt_pk_f16_f32 v3, v6, v7
	v_pk_fma_f32 v[6:7], v[12:13], s[10:11], v[194:195] op_sel_hi:[1,0,1]
	v_cvt_pk_f16_f32 v4, v4, v5
	v_cvt_pk_f16_f32 v5, v6, v7
	v_bitop3_b32 v6, v62, v120, 2 bitop3:0x36
	v_lshlrev_b32_e32 v6, 4, v6
	v_or_b32_e32 v7, v63, v6
	ds_write_b64 v7, v[2:3]
	v_or_b32_e32 v2, v58, v6
	ds_write_b64 v2, v[4:5]
	v_pk_fma_f32 v[2:3], v[30:31], s[10:11], v[196:197] op_sel_hi:[1,0,1]
	v_pk_fma_f32 v[6:7], v[32:33], s[10:11], v[198:199] op_sel_hi:[1,0,1]
	v_cvt_pk_f16_f32 v2, v2, v3
	v_pk_fma_f32 v[4:5], v[14:15], s[10:11], v[196:197] op_sel_hi:[1,0,1]
	v_cvt_pk_f16_f32 v3, v6, v7
	v_pk_fma_f32 v[6:7], v[16:17], s[10:11], v[198:199] op_sel_hi:[1,0,1]
	v_cvt_pk_f16_f32 v4, v4, v5
	v_cvt_pk_f16_f32 v5, v6, v7
	v_bitop3_b32 v6, v62, v120, 3 bitop3:0x36
	v_lshlrev_b32_e32 v6, 4, v6
	v_or_b32_e32 v7, v63, v6
	ds_write_b64 v7, v[2:3]
	v_or_b32_e32 v2, v58, v6
	ds_write_b64 v2, v[4:5]
	s_waitcnt vmcnt(0) lgkmcnt(0)
	s_barrier
	v_and_b32_e32 v236, 1, v101
	v_lshrrev_b32_e32 v237, 1, v101
	v_xor_b32_e32 v237, v237, v236
	v_lshl_or_b32 v236, v236, 1, v237
	v_lshrrev_b32_e32 v27, 8, v0
	v_lshrrev_b32_e32 v3, 3, v0
	v_and_b32_e32 v3, 16, v3
	v_mul_u32_u24_e32 v28, 0x60, v27
	v_lshlrev_b32_e32 v26, 5, v27
	v_or_b32_e32 v146, v3, v100
	v_or_b32_e32 v147, v28, v100
	v_or_b32_e32 v4, v146, v26
	v_lshlrev_b32_e32 v209, 2, v4
	v_add_u32_e32 v209, 0x27800, v209
	v_lshlrev_b32_e32 v4, 8, v4
	v_or_b32_e32 v5, 0x18000, v4
	v_bitop3_b32 v11, v236, v120, 12 bitop3:0x36
	v_or_b32_e32 v95, 0x1c000, v4
	v_lshlrev_b32_e32 v29, 3, v101
	v_bitop3_b32 v6, v236, v94, v61 bitop3:0x1e
	v_bitop3_b32 v8, v236, v120, 4 bitop3:0x36
	v_bitop3_b32 v10, v236, v120, 8 bitop3:0x36
	v_lshlrev_b32_e32 v94, 4, v11
	v_lshlrev_b32_e32 v6, 4, v6
	v_lshlrev_b32_e32 v8, 4, v8
	v_lshlrev_b32_e32 v58, 4, v10
	v_or_b32_e32 v7, v5, v6
	v_or_b32_e32 v9, v5, v8
	v_or_b32_e32 v10, v5, v58
	v_or_b32_e32 v5, v5, v94
	v_or_b32_e32 v6, v95, v6
	v_or_b32_e32 v60, v95, v8
	ds_read_b128 v[22:25], v7
	ds_read_b128 v[18:21], v9
	ds_read_b128 v[14:17], v10
	ds_read_b128 v[10:13], v5
	ds_read_b128 v[6:9], v6
	ds_read_b128 v[2:5], v60
	v_bfe_u32 v103, v0, 6, 1
	s_movk_i32 s5, 0x2000
	v_mad_u32_u24 v44, v103, 48, v147
	v_lshlrev_b32_e32 v60, 8, v44
	v_lshlrev_b32_e32 v44, 2, v44
	v_or_b32_e32 v35, v95, v58
	v_lshlrev_b32_e32 v58, 14, v99
	v_and_b32_e32 v44, 12, v44
	v_or_b32_e32 v56, v44, v61
	v_bitop3_b32 v44, v236, v44, v61 bitop3:0x1e
	v_lshl_add_u64 v[32:33], s[8:9], 0, v[58:59]
	v_lshlrev_b32_e32 v58, 4, v98
	v_or_b32_e32 v36, v95, v94
	v_lshl_add_u64 v[88:89], v[32:33], 0, v[58:59]
	v_lshl_or_b32 v57, v44, 4, v60
	ds_read_b128 v[40:43], v35
	ds_read_b128 v[106:109], v36
	global_load_dwordx4 v[36:39], v[88:89], off
	global_load_dwordx4 v[32:35], v[88:89], off offset:1024
	ds_read_b128 v[44:47], v57
	v_bitop3_b32 v48, v236, v56, 4 bitop3:0x36
	v_lshl_or_b32 v62, v48, 4, v60
	ds_read_b128 v[48:51], v62
	v_bitop3_b32 v52, v236, v56, 8 bitop3:0x36
	v_lshl_or_b32 v63, v52, 4, v60
	ds_read_b128 v[52:55], v63
	s_waitcnt lgkmcnt(0)
	v_mfma_f32_16x16x32_f16 v[44:47], v[44:47], v[22:25], 0
	v_bitop3_b32 v64, v236, v56, 12 bitop3:0x36
	ds_read_b128 v[56:59], v57 offset:49152
	v_lshl_or_b32 v60, v64, 4, v60
	v_mfma_f32_16x16x32_f16 v[44:47], v[48:51], v[18:21], v[44:47]
	ds_read_b128 v[68:71], v60
	ds_read_b128 v[72:75], v62 offset:49152
	v_mad_u32_u24 v104, v103, 3, 1
	v_lshlrev_b32_e32 v132, 4, v104
	v_mfma_f32_16x16x32_f16 v[44:47], v[52:55], v[14:17], v[44:47]
	v_add_u32_e32 v52, v132, v147
	global_load_dwordx4 v[64:67], v[88:89], off offset:2048
	global_load_dwordx4 v[48:51], v[88:89], off offset:3072
	ds_read_b128 v[76:79], v63 offset:49152
	ds_read_b128 v[80:83], v60 offset:49152
	s_waitcnt lgkmcnt(3)
	v_mfma_f32_16x16x32_f16 v[44:47], v[68:71], v[10:13], v[44:47]
	v_lshlrev_b32_e32 v60, 8, v52
	v_lshlrev_b32_e32 v52, 2, v52
	v_and_b32_e32 v52, 12, v52
	v_mfma_f32_16x16x32_f16 v[44:47], v[56:59], v[6:9], v[44:47]
	v_or_b32_e32 v62, v52, v61
	v_bitop3_b32 v52, v236, v52, v61 bitop3:0x1e
	v_lshl_or_b32 v63, v52, 4, v60
	s_waitcnt lgkmcnt(2)
	v_mfma_f32_16x16x32_f16 v[44:47], v[72:75], v[2:5], v[44:47]
	ds_read_b128 v[52:55], v63
	v_bitop3_b32 v56, v236, v62, 4 bitop3:0x36
	v_lshl_or_b32 v84, v56, 4, v60
	s_waitcnt lgkmcnt(2)
	v_mfma_f32_16x16x32_f16 v[44:47], v[76:79], v[40:43], v[44:47]
	ds_read_b128 v[56:59], v84
	v_bitop3_b32 v68, v236, v62, 8 bitop3:0x36
	v_lshl_or_b32 v85, v68, 4, v60
	s_waitcnt lgkmcnt(2)
	v_mfma_f32_16x16x32_f16 v[110:113], v[80:83], v[106:109], v[44:47]
	ds_read_b128 v[68:71], v63 offset:49152
	v_bitop3_b32 v62, v236, v62, 12 bitop3:0x36
	v_lshl_or_b32 v60, v62, 4, v60
	ds_read_b128 v[44:47], v85
	s_waitcnt lgkmcnt(3)
	v_mfma_f32_16x16x32_f16 v[52:55], v[52:55], v[22:25], 0
	ds_read_b128 v[72:75], v60
	ds_read_b128 v[76:79], v84 offset:49152
	v_mad_u32_u24 v105, v103, 3, 2
	v_lshlrev_b32_e32 v133, 4, v105
	s_waitcnt lgkmcnt(4)
	v_mfma_f32_16x16x32_f16 v[52:55], v[56:59], v[18:21], v[52:55]
	ds_read_b128 v[56:59], v85 offset:49152
	v_add_co_u32_e32 v114, vcc, s15, v88
	s_waitcnt lgkmcnt(3)
	v_mfma_f32_16x16x32_f16 v[44:47], v[44:47], v[14:17], v[52:55]
	v_addc_co_u32_e32 v115, vcc, 0, v89, vcc
	s_waitcnt lgkmcnt(2)
	v_mfma_f32_16x16x32_f16 v[44:47], v[72:75], v[10:13], v[44:47]
	ds_read_b128 v[52:55], v60 offset:49152
	v_add_u32_e32 v60, v133, v147
	v_lshlrev_b32_e32 v72, 8, v60
	v_lshlrev_b32_e32 v60, 2, v60
	v_mfma_f32_16x16x32_f16 v[44:47], v[68:71], v[6:9], v[44:47]
	v_and_b32_e32 v60, 12, v60
	v_or_b32_e32 v68, v60, v61
	v_bitop3_b32 v60, v236, v60, v61 bitop3:0x1e
	v_lshl_or_b32 v69, v60, 4, v72
	s_waitcnt lgkmcnt(2)
	v_mfma_f32_16x16x32_f16 v[44:47], v[76:79], v[2:5], v[44:47]
	ds_read_b128 v[60:63], v69
	v_bitop3_b32 v70, v236, v68, 4 bitop3:0x36
	v_lshl_or_b32 v70, v70, 4, v72
	s_waitcnt lgkmcnt(2)
	v_mfma_f32_16x16x32_f16 v[44:47], v[56:59], v[40:43], v[44:47]
	ds_read_b128 v[56:59], v70
	v_bitop3_b32 v71, v236, v68, 8 bitop3:0x36
	v_lshl_or_b32 v71, v71, 4, v72
	s_waitcnt lgkmcnt(1)
	v_mfma_f32_16x16x32_f16 v[22:25], v[60:63], v[22:25], 0
	v_bitop3_b32 v60, v236, v68, 12 bitop3:0x36
	v_lshl_or_b32 v68, v60, 4, v72
	ds_read_b32 v210, v209
	v_mfma_f32_16x16x32_f16 v[126:129], v[52:55], v[106:109], v[44:47]
	s_nop 2
	ds_read_b128 v[44:47], v71
	ds_read_b128 v[52:55], v69 offset:49152
	ds_read_b128 v[60:63], v70 offset:49152
	s_waitcnt lgkmcnt(4)
	v_mfma_f32_16x16x32_f16 v[18:21], v[56:59], v[18:21], v[22:25]
	ds_read_b128 v[56:59], v71 offset:49152
	s_nop 1
	ds_read_b128 v[22:25], v68
	s_waitcnt lgkmcnt(4)
	v_mfma_f32_16x16x32_f16 v[14:17], v[44:47], v[14:17], v[18:21]
	v_add_co_u32_e32 v44, vcc, s5, v88
	s_movk_i32 s5, 0x3000
	s_nop 0
	ds_read_b128 v[18:21], v68 offset:49152
	s_waitcnt lgkmcnt(1)
	v_mfma_f32_16x16x32_f16 v[10:13], v[22:25], v[10:13], v[14:17]
	v_addc_co_u32_e32 v45, vcc, 0, v89, vcc
	global_load_dwordx4 v[84:87], v[114:115], off offset:1024
	global_load_dwordx4 v[80:83], v[114:115], off offset:2048
	global_load_dwordx4 v[92:95], v[44:45], off offset:-4096
	global_load_dwordx4 v[76:79], v[44:45], off
	v_mfma_f32_16x16x32_f16 v[6:9], v[52:55], v[6:9], v[10:13]
	global_load_dwordx4 v[72:75], v[44:45], off offset:1024
	global_load_dwordx4 v[68:71], v[44:45], off offset:2048
	global_load_dwordx4 v[52:55], v[44:45], off offset:3072
	v_mov_b32_e32 v13, 0xff61b1e6
	v_mfma_f32_16x16x32_f16 v[2:5], v[60:63], v[2:5], v[6:9]
	s_nop 2
	v_add_co_u32_e32 v6, vcc, s5, v88
	v_mfma_f32_16x16x32_f16 v[2:5], v[56:59], v[40:43], v[2:5]
	s_nop 0
	v_addc_co_u32_e32 v7, vcc, 0, v89, vcc
	global_load_dwordx4 v[88:91], v[114:115], off offset:3072
	global_load_dwordx4 v[60:63], v[6:7], off
	global_load_dwordx4 v[56:59], v[6:7], off offset:1024
	global_load_dwordx4 v[44:47], v[6:7], off offset:2048
	global_load_dwordx4 v[40:43], v[6:7], off offset:3072
	s_waitcnt lgkmcnt(0)
	v_mfma_f32_16x16x32_f16 v[16:19], v[18:21], v[106:109], v[2:5]
	s_mov_b32 s5, 0xff61b1e6
	s_nop 0
	v_or_b32_e32 v3, s14, v146
	v_mov_b32_e32 v4, 0x7df
	v_med3_u32 v3, v3, 32, v4
	v_or_b32_e32 v4, v97, v102
	v_sub_u32_e32 v3, v4, v3
	v_add_f32_e32 v2, s32, v210
	v_add_u32_e32 v3, 32, v3
	v_mad_u32_u24 v4, v103, 48, v3
	s_movk_i32 s4, 0x41
	v_add_f32_e32 v5, v2, v110
	v_mul_f32_e32 v5, 0x3db8aa3b, v5
	v_cmp_gt_u32_e32 vcc, s4, v4
	v_add_u32_e32 v6, 1, v4
	v_add_f32_e32 v7, v2, v111
	v_cndmask_b32_e32 v5, v13, v5, vcc
	v_mul_f32_e32 v7, 0x3db8aa3b, v7
	v_cmp_gt_u32_e32 vcc, s4, v6
	v_add_u32_e32 v8, 2, v4
	v_add_f32_e32 v9, v2, v112
	v_cndmask_b32_e32 v6, v13, v7, vcc
	v_mul_f32_e32 v9, 0x3db8aa3b, v9
	v_cmp_gt_u32_e32 vcc, s4, v8
	v_add_u32_e32 v4, 3, v4
	v_max3_f32 v7, v5, s5, v6
	v_cndmask_b32_e32 v8, v13, v9, vcc
	v_add_f32_e32 v9, v2, v113
	v_mul_f32_e32 v9, 0x3db8aa3b, v9
	v_cmp_gt_u32_e32 vcc, s4, v4
	v_add_u32_e32 v11, v3, v132
	v_add_f32_e32 v12, v2, v127
	v_cndmask_b32_e32 v10, v13, v9, vcc
	v_max3_f32 v4, v7, v8, v10
	v_add_f32_e32 v7, v2, v126
	v_mul_f32_e32 v7, 0x3db8aa3b, v7
	v_cmp_gt_u32_e32 vcc, s4, v11
	v_add_u32_e32 v9, 1, v11
	v_mul_f32_e32 v12, 0x3db8aa3b, v12
	v_cndmask_b32_e32 v7, v13, v7, vcc
	v_cmp_gt_u32_e32 vcc, s4, v9
	v_add_f32_e32 v14, v2, v128
	v_mul_f32_e32 v14, 0x3db8aa3b, v14
	v_cndmask_b32_e32 v9, v13, v12, vcc
	v_add_u32_e32 v12, 2, v11
	v_cmp_gt_u32_e32 vcc, s4, v12
	v_add_u32_e32 v11, 3, v11
	v_add_u32_e32 v3, v3, v133
	v_cndmask_b32_e32 v12, v13, v14, vcc
	v_add_f32_e32 v14, v2, v129
	v_mul_f32_e32 v14, 0x3db8aa3b, v14
	v_cmp_gt_u32_e32 vcc, s4, v11
	v_add_f32_e32 v11, v2, v16
	v_mul_f32_e32 v11, 0x3db8aa3b, v11
	v_cndmask_b32_e32 v15, v13, v14, vcc
	v_cmp_gt_u32_e32 vcc, s4, v3
	v_add_u32_e32 v14, 1, v3
	v_add_f32_e32 v16, v2, v17
	v_cndmask_b32_e32 v11, v13, v11, vcc
	v_mul_f32_e32 v16, 0x3db8aa3b, v16
	v_cmp_gt_u32_e32 vcc, s4, v14
	v_add_f32_e32 v17, v2, v18
	v_max3_f32 v4, v4, v7, v9
	v_cndmask_b32_e32 v14, v13, v16, vcc
	v_add_u32_e32 v16, 2, v3
	v_mul_f32_e32 v17, 0x3db8aa3b, v17
	v_cmp_gt_u32_e32 vcc, s4, v16
	v_add_u32_e32 v3, 3, v3
	v_add_f32_e32 v2, v2, v19
	v_max3_f32 v4, v4, v12, v15
	v_cndmask_b32_e32 v16, v13, v17, vcc
	v_mul_f32_e32 v2, 0x3db8aa3b, v2
	v_cmp_gt_u32_e32 vcc, s4, v3
	v_max3_f32 v4, v4, v11, v14
	v_lshlrev_b32_e32 v126, 5, v99
	v_cndmask_b32_e32 v17, v13, v2, vcc
	v_max3_f32 v2, v4, v16, v17
	v_mov_b32_e32 v3, v2
	v_lshlrev_b32_e32 v127, 2, v119
	v_lshrrev_b32_e32 v4, 7, v0
	v_cmp_gt_u32_e32 vcc, 16, v98
	v_permlane16_swap_b32_e32 v3, v2
	v_max_f32_e32 v2, v2, v3
	v_mov_b32_e32 v3, v2
	s_nop 1
	v_permlane32_swap_b32_e32 v3, v2
	v_max_f32_e32 v13, v2, v3
	v_and_b32_e32 v2, 0x180, v0
	v_or_b32_e32 v2, 0x23400, v2
	v_lshlrev_b32_e32 v3, 2, v100
	s_and_saveexec_b64 s[4:5], vcc
	v_lshlrev_b32_e32 v18, 6, v103
	v_add3_u32 v18, v2, v18, v3
	ds_write_b32 v18, v13
	s_or_b64 exec, exec, s[4:5]
	v_lshlrev_b32_e32 v18, 4, v103
	v_bitop3_b32 v19, v18, 16, v100 bitop3:0x36
	v_lshl_add_u32 v2, v19, 2, v2
	s_waitcnt lgkmcnt(0)
	s_barrier
	ds_read_b32 v19, v2
	v_max_f32_e32 v13, v13, v13
	v_mul_u32_u24_e32 v20, 0xd00, v4
	v_or_b32_e32 v2, 1, v124
	s_waitcnt lgkmcnt(0)
	v_max_f32_e32 v19, v19, v19
	v_max_f32_e32 v19, v13, v19
	v_sub_f32_e32 v5, v5, v19
	v_exp_f32_e32 v5, v5
	v_sub_f32_e32 v6, v6, v19
	v_exp_f32_e32 v6, v6
	v_sub_f32_e32 v8, v8, v19
	v_mul_u32_u24_e32 v13, 0xd0, v100
	v_exp_f32_e32 v8, v8
	v_sub_f32_e32 v10, v10, v19
	v_add3_u32 v20, v13, v20, v29
	v_exp_f32_e32 v10, v10
	v_or_b32_e32 v22, 0x20000, v20
	v_add_f32_e32 v20, 0, v5
	v_add_f32_e32 v20, v20, v6
	v_add_f32_e32 v20, v20, v8
	v_add_f32_e32 v23, v20, v10
	v_cvt_pk_f16_f32 v21, v8, v10
	v_cvt_pk_f16_f32 v20, v5, v6
	v_mad_u32_u24 v5, v103, s16, v22
	ds_write_b64 v5, v[20:21]
	v_sub_f32_e32 v5, v7, v19
	v_exp_f32_e32 v5, v5
	v_sub_f32_e32 v6, v9, v19
	v_exp_f32_e32 v6, v6
	v_sub_f32_e32 v7, v12, v19
	v_exp_f32_e32 v7, v7
	v_sub_f32_e32 v8, v15, v19
	v_exp_f32_e32 v8, v8
	v_sub_f32_e32 v10, v11, v19
	v_add_f32_e32 v9, v23, v5
	v_exp_f32_e32 v10, v10
	v_sub_f32_e32 v11, v14, v19
	v_add_f32_e32 v9, v9, v6
	v_exp_f32_e32 v11, v11
	v_sub_f32_e32 v12, v16, v19
	v_add_f32_e32 v9, v9, v7
	v_exp_f32_e32 v12, v12
	v_sub_f32_e32 v14, v17, v19
	v_add_f32_e32 v9, v9, v8
	v_exp_f32_e32 v14, v14
	v_add_f32_e32 v9, v9, v10
	v_add_f32_e32 v9, v9, v11
	v_add_f32_e32 v9, v9, v12
	v_add_f32_e32 v9, v9, v14
	v_mov_b32_e32 v15, v9
	v_cvt_pk_f16_f32 v7, v7, v8
	v_cvt_pk_f16_f32 v6, v5, v6
	v_lshl_add_u32 v5, v104, 5, v22
	ds_write_b64 v5, v[6:7]
	v_permlane16_swap_b32_e32 v15, v9
	v_add_f32_e32 v5, v9, v15
	v_mov_b32_e32 v6, v5
	s_movk_i32 s7, 0xd00
	s_mov_b32 s6, 0x20000
	v_cvt_pk_f16_f32 v9, v12, v14
	v_cvt_pk_f16_f32 v8, v10, v11
	v_lshl_add_u32 v7, v105, 5, v22
	ds_write_b64 v7, v[8:9]
	v_permlane32_swap_b32_e32 v6, v5
	s_and_saveexec_b64 s[4:5], vcc
	s_cbranch_execz .LBB1_4
	v_lshlrev_b32_e32 v4, 5, v4
	v_or_b32_e32 v7, v18, v100
	v_lshlrev_b32_e32 v4, 2, v4
	v_lshlrev_b32_e32 v7, 2, v7
	s_mov_b32 s8, 0x23600
	v_add3_u32 v4, v7, v4, s8
	v_add_f32_e32 v5, v5, v6
	ds_write_b32 v4, v5
.LBB1_4:
	s_or_b64 exec, exec, s[4:5]
	v_lshl_or_b32 v4, v27, 1, v96
	v_lshl_or_b32 v3, v4, 7, v3
	v_or_b32_e32 v5, 0x23600, v3
	v_or_b32_e32 v3, 0x23640, v3
	s_waitcnt lgkmcnt(0)
	s_barrier
	ds_read_b32 v5, v5
	ds_read_b32 v3, v3
	v_mad_u32_u24 v4, v4, s7, v13
	v_lshl_add_u32 v4, v119, 4, v4
	v_or_b32_e32 v6, 0x20000, v4
	ds_read_b128 v[16:19], v6
	s_waitcnt lgkmcnt(1)
	v_add_f32_e32 v3, v5, v3
	v_add_u32_e32 v5, 0x20020, v4
	v_add_u32_e32 v6, 0x20040, v4
	ds_read_b128 v[112:115], v5
	ds_read_b128 v[108:111], v6
	v_add_u32_e32 v5, 0x20060, v4
	v_add_u32_e32 v6, 0x20080, v4
	v_lshlrev_b32_e32 v7, 1, v101
	ds_read_b128 v[104:107], v5
	ds_read_b128 v[96:99], v6
	v_lshrrev_b32_e32 v5, 2, v100
	v_or_b32_e32 v6, v28, v125
	v_and_b32_e32 v7, 2, v7
	v_bfe_u32 v8, v0, 1, 1
	v_and_b32_e32 v164, 8, v121
	v_bfe_i32 v9, v0, 7, 1
	v_or3_b32 v8, v8, v7, v164
	v_and_b32_e32 v0, 12, v0
	v_add_lshl_u32 v10, v6, v5, 8
	v_or_b32_e32 v5, v6, v5
	v_and_b32_e32 v9, 0xc000, v9
	v_lshlrev_b32_e32 v12, 8, v5
	v_bitop3_b32 v5, v0, v8, v124 bitop3:0x36
	v_lshl_or_b32 v13, v5, 4, v9
	v_bitop3_b32 v6, v0, v8, v2 bitop3:0x36
	v_or_b32_e32 v15, 0x1000, v12
	v_lshl_or_b32 v14, v6, 4, v9
	v_add_u32_e32 v7, v13, v15
	v_or_b32_e32 v24, 0x1400, v12
	v_or_b32_e32 v20, v7, v1
	v_add_u32_e32 v7, v14, v24
	v_add_u32_e32 v25, 0x2000, v10
	v_add_u32_e32 v5, v13, v12
	v_add_u32_e32 v6, v14, v12
	v_or_b32_e32 v22, v7, v1
	v_add_u32_e32 v7, v13, v25
	v_add_u32_e32 v150, 0x3000, v10
	v_or_b32_e32 v8, 4, v8
	v_add_u32_e32 v4, 0x200a0, v4
	v_or_b32_e32 v5, v5, v1
	v_or_b32_e32 v6, v6, v1
	v_or_b32_e32 v27, v7, v1
	v_add_u32_e32 v31, v13, v150
	v_add_u32_e32 v151, 0x3400, v10
	v_bitop3_b32 v124, v0, v8, v124 bitop3:0x36
	v_bitop3_b32 v0, v0, v8, v2 bitop3:0x36
	ds_read_b128 v[100:103], v4
	ds_read_b64_tr_b16 v[4:5], v5
	ds_read_b64_tr_b16 v[6:7], v6 offset:1024
	ds_read_b64_tr_b16 v[20:21], v20
	ds_read_b64_tr_b16 v[22:23], v22
	ds_read_b64_tr_b16 v[28:29], v27
	v_add_u32_e32 v27, 0x2400, v10
	v_or_b32_e32 v128, v31, v1
	v_add_u32_e32 v31, v14, v151
	v_add_u32_e32 v152, 0x4000, v10
	v_add_u32_e32 v158, 0x4400, v10
	v_lshl_or_b32 v124, v124, 4, v9
	v_lshl_or_b32 v0, v0, 4, v9
	v_add_u32_e32 v11, 0x5000, v10
	v_add_u32_e32 v30, v14, v27
	v_or_b32_e32 v130, v31, v1
	v_add_u32_e32 v31, v13, v152
	v_add_u32_e32 v134, v14, v158
	v_add_u32_e32 v10, 0x5400, v10
	v_add_u32_e32 v135, v124, v12
	v_add_u32_e32 v2, v0, v12
	v_add_u32_e32 v8, v124, v15
	v_or_b32_e32 v30, v30, v1
	v_or_b32_e32 v132, v31, v1
	v_or_b32_e32 v134, v134, v1
	v_add_u32_e32 v13, v13, v11
	v_add_u32_e32 v14, v14, v10
	v_or_b32_e32 v140, v135, v1
	v_or_b32_e32 v2, v2, v1
	v_or_b32_e32 v8, v8, v1
	v_add_u32_e32 v9, v0, v24
	v_add_u32_e32 v12, v124, v25
	ds_read_b64_tr_b16 v[30:31], v30
	ds_read_b64_tr_b16 v[128:129], v128
	ds_read_b64_tr_b16 v[130:131], v130
	ds_read_b64_tr_b16 v[132:133], v132
	v_or_b32_e32 v13, v13, v1
	v_or_b32_e32 v14, v14, v1
	ds_read_b64_tr_b16 v[134:135], v134
	ds_read_b64_tr_b16 v[136:137], v13
	ds_read_b64_tr_b16 v[138:139], v14
	ds_read_b64_tr_b16 v[140:141], v140
	v_or_b32_e32 v9, v9, v1
	v_or_b32_e32 v12, v12, v1
	ds_read_b64_tr_b16 v[142:143], v2 offset:1024
	ds_read_b64_tr_b16 v[144:145], v8
	ds_read_b64_tr_b16 v[146:147], v9
	ds_read_b64_tr_b16 v[148:149], v12
	v_add_u32_e32 v2, v0, v27
	v_add_u32_e32 v8, v124, v150
	v_or_b32_e32 v2, v2, v1
	v_or_b32_e32 v8, v8, v1
	v_add_u32_e32 v9, v0, v151
	v_add_u32_e32 v12, v124, v152
	v_or_b32_e32 v9, v9, v1
	v_or_b32_e32 v12, v12, v1
	ds_read_b64_tr_b16 v[150:151], v2
	ds_read_b64_tr_b16 v[152:153], v8
	ds_read_b64_tr_b16 v[154:155], v9
	ds_read_b64_tr_b16 v[156:157], v12
	v_add_u32_e32 v2, v0, v158
	v_add_u32_e32 v8, v124, v11
	v_add_u32_e32 v0, v0, v10
	v_or_b32_e32 v2, v2, v1
	v_or_b32_e32 v8, v8, v1
	v_or_b32_e32 v0, v0, v1
	v_div_scale_f32 v1, s[8:9], v3, v3, 1.0
	v_rcp_f32_e32 v9, v1
	ds_read_b64_tr_b16 v[158:159], v2
	ds_read_b64_tr_b16 v[160:161], v8
	ds_read_b64_tr_b16 v[162:163], v0
	s_mov_b32 s4, 0xc000
	s_movk_i32 s5, 0x4000
	v_fma_f32 v0, -v1, v9, 1.0
	v_fmac_f32_e32 v9, v0, v9
	v_div_scale_f32 v0, vcc, 1.0, v3, 1.0
	v_mul_f32_e32 v2, v0, v9
	v_fma_f32 v8, -v1, v2, v0
	v_fmac_f32_e32 v2, v8, v9
	v_fma_f32 v0, -v1, v2, v0
	v_div_fmas_f32 v0, v0, v9, v2
	v_div_fixup_f32 v124, v0, v3, 1.0
	s_waitcnt lgkmcnt(14)
	v_mfma_f32_32x32x16_f16 v[0:15], v[4:7], v[16:19], 0
	s_mov_b32 s7, 0x18000
	v_lshlrev_b32_e32 v172, 2, v126
	v_mov_b32_e32 v173, 0
	v_mfma_f32_32x32x16_f16 v[0:15], v[20:23], v[112:115], v[0:15]
	v_or_b32_e32 v20, v26, v116
	v_and_b32_e32 v21, 0x4000, v118
	v_lshl_or_b32 v20, v20, 8, v21
	v_bitop3_b32 v118, v121, v120, 8 bitop3:0x6c
	v_or3_b32 v121, v20, v125, s7
	v_mfma_f32_32x32x16_f16 v[0:15], v[28:31], v[108:111], v[0:15]
	v_mfma_f32_32x32x16_f16 v[0:15], v[128:131], v[104:107], v[0:15]
	v_mfma_f32_32x32x16_f16 v[0:15], v[132:135], v[96:99], v[0:15]
	s_waitcnt lgkmcnt(12)
	v_mfma_f32_32x32x16_f16 v[0:15], v[136:139], v[100:103], v[0:15]
	s_nop 11
	v_fma_mixlo_f16 v20, v124, v0, 0
	v_mov_b32_e32 v0, v1
	v_mov_b32_e32 v1, v2
	v_pk_mul_f32 v[0:1], v[124:125], v[0:1] op_sel_hi:[0,1]
	v_cvt_pk_f16_f32 v1, v0, v1
	v_pack_b32_f16 v0, v20, v1
	s_waitcnt lgkmcnt(10)
	v_mfma_f32_32x32x16_f16 v[16:31], v[140:143], v[16:19], 0
	v_fma_mixlo_f16 v2, v124, v3, 0
	v_alignbit_b32 v1, v2, v1, 16
	v_lshl_or_b32 v2, v118, 4, v121
	ds_write_b64 v2, v[0:1]
	v_mov_b32_e32 v0, v5
	v_mov_b32_e32 v1, v6
	v_pk_mul_f32 v[0:1], v[124:125], v[0:1] op_sel_hi:[0,1]
	s_waitcnt lgkmcnt(9)
	v_mfma_f32_32x32x16_f16 v[16:31], v[144:147], v[112:115], v[16:31]
	v_fma_mixlo_f16 v2, v124, v4, 0
	v_cvt_pk_f16_f32 v1, v0, v1
	v_pack_b32_f16 v0, v2, v1
	v_fma_mixlo_f16 v2, v124, v7, 0
	v_alignbit_b32 v1, v2, v1, 16
	v_bitop3_b32 v2, v164, v120, 1 bitop3:0x36
	v_lshl_or_b32 v2, v2, 4, v121
	s_waitcnt lgkmcnt(7)
	v_mfma_f32_32x32x16_f16 v[16:31], v[148:151], v[108:111], v[16:31]
	ds_write_b64 v2, v[0:1]
	v_mov_b32_e32 v0, v9
	v_mov_b32_e32 v1, v10
	v_mul_f32_e64 v0, v124, v0
	v_mul_f32_e64 v1, v124, v1
	v_fma_mixlo_f16 v2, v124, v8, 0
	v_cvt_pk_f16_f32 v1, v0, v1
	v_pack_b32_f16 v0, v2, v1
	s_waitcnt lgkmcnt(6)
	v_mfma_f32_32x32x16_f16 v[16:31], v[152:155], v[104:107], v[16:31]
	v_fma_mixlo_f16 v2, v124, v11, 0
	v_alignbit_b32 v1, v2, v1, 16
	v_bitop3_b32 v2, v164, v120, 2 bitop3:0x36
	v_lshl_or_b32 v2, v2, 4, v121
	ds_write_b64 v2, v[0:1]
	v_mov_b32_e32 v0, v13
	v_mov_b32_e32 v1, v14
	s_waitcnt lgkmcnt(5)
	v_mfma_f32_32x32x16_f16 v[16:31], v[156:159], v[96:99], v[16:31]
	v_mul_f32_e64 v0, v124, v0
	v_mul_f32_e64 v1, v124, v1
	v_fma_mixlo_f16 v2, v124, v12, 0
	v_cvt_pk_f16_f32 v1, v0, v1
	v_pack_b32_f16 v0, v2, v1
	v_fma_mixlo_f16 v2, v124, v15, 0
	v_alignbit_b32 v1, v2, v1, 16
	v_bitop3_b32 v2, v164, v120, 3 bitop3:0x36
	s_waitcnt lgkmcnt(3)
	v_mfma_f32_32x32x16_f16 v[16:31], v[160:163], v[100:103], v[16:31]
	v_lshl_or_b32 v2, v2, 4, v121
	ds_write_b64 v2, v[0:1]
	s_nop 9
	v_mov_b32_e32 v0, v17
	v_mov_b32_e32 v1, v18
	v_pk_mul_f32 v[0:1], v[124:125], v[0:1] op_sel_hi:[0,1]
	v_fma_mixlo_f16 v2, v124, v16, 0
	v_cvt_pk_f16_f32 v1, v0, v1
	v_pack_b32_f16 v0, v2, v1
	v_fma_mixlo_f16 v2, v124, v19, 0
	v_alignbit_b32 v1, v2, v1, 16
	v_bitop3_b32 v2, v164, v120, 4 bitop3:0x36
	v_lshl_or_b32 v2, v2, 4, v121
	ds_write_b64 v2, v[0:1]
	v_mov_b32_e32 v0, v21
	v_mov_b32_e32 v1, v22
	v_pk_mul_f32 v[0:1], v[124:125], v[0:1] op_sel_hi:[0,1]
	v_fma_mixlo_f16 v2, v124, v20, 0
	v_cvt_pk_f16_f32 v1, v0, v1
	v_pack_b32_f16 v0, v2, v1
	v_fma_mixlo_f16 v2, v124, v23, 0
	v_alignbit_b32 v1, v2, v1, 16
	v_bitop3_b32 v2, v164, v120, 5 bitop3:0x36
	v_lshl_or_b32 v2, v2, 4, v121
	ds_write_b64 v2, v[0:1]
	v_mov_b32_e32 v0, v25
	v_mov_b32_e32 v1, v26
	v_pk_mul_f32 v[0:1], v[124:125], v[0:1] op_sel_hi:[0,1]
	v_fma_mixlo_f16 v2, v124, v24, 0
	v_cvt_pk_f16_f32 v1, v0, v1
	v_pack_b32_f16 v0, v2, v1
	v_fma_mixlo_f16 v2, v124, v27, 0
	v_alignbit_b32 v1, v2, v1, 16
	v_bitop3_b32 v2, v164, v120, 6 bitop3:0x36
	v_lshl_or_b32 v2, v2, 4, v121
	ds_write_b64 v2, v[0:1]
	v_mov_b32_e32 v0, v29
	v_mov_b32_e32 v1, v30
	v_pk_mul_f32 v[0:1], v[124:125], v[0:1] op_sel_hi:[0,1]
	v_fma_mixlo_f16 v2, v124, v28, 0
	v_cvt_pk_f16_f32 v1, v0, v1
	v_pack_b32_f16 v0, v2, v1
	v_fma_mixlo_f16 v2, v124, v31, 0
	v_alignbit_b32 v1, v2, v1, 16
	v_bitop3_b32 v2, v164, v120, 7 bitop3:0x36
	v_lshl_or_b32 v2, v2, 4, v121
	ds_write_b64 v2, v[0:1]
	v_lshl_add_u64 v[0:1], s[0:1], 0, v[172:173]
	v_lshlrev_b32_e32 v172, 2, v127
	v_lshl_add_u64 v[0:1], v[0:1], 0, v[172:173]
	s_waitcnt lgkmcnt(0)
	s_barrier
	v_and_b32_e32 v245, 15, v116
	v_lshrrev_b32_e32 v246, 4, v116
	v_lshl_or_b32 v246, v119, 1, v246
	v_lshrrev_b32_e32 v250, 5, v126
	v_and_b32_e32 v250, 7, v250
	v_and_b32_e32 v247, 1, v246
	v_lshrrev_b32_e32 v248, 1, v246
	v_xor_b32_e32 v248, v248, v247
	v_lshl_or_b32 v247, v247, 1, v248
	v_and_b32_e32 v248, 3, v245
	v_lshrrev_b32_e32 v249, 2, v245
	v_lshl_or_b32 v248, v248, 2, v249
	v_xor_b32_e32 v247, v247, v248
	v_lshlrev_b32_e32 v240, 8, v245
	v_lshl_or_b32 v240, v247, 4, v240
	v_add_u32_e32 v240, 0x18000, v240
	v_xor_b32_e32 v241, 64, v240
	v_xor_b32_e32 v242, 0x80, v240
	v_xor_b32_e32 v243, 0xc0, v240
	v_lshlrev_b32_e32 v249, 7, v250
	v_lshl_or_b32 v249, v246, 4, v249
	v_and_b32_e32 v249, 0x3f0, v249
	global_load_dwordx4 v[96:99], v249, s[34:35]
	global_load_dwordx4 v[100:103], v249, s[34:35] offset:64
	v_lshlrev_b32_e32 v244, 19, v250
	v_lshl_or_b32 v244, v246, 16, v244
	v_lshl_or_b32 v244, v245, 3, v244
	v_and_b32_e32 v244, 0x3fff78, v244
	s_lshl_b64 s[22:23], s[2:3], 22
	s_add_u32 s22, s22, s30
	s_addc_u32 s23, s23, s31
	s_lshl_b32 s24, s14, 3
	s_add_u32 s22, s22, s24
	s_addc_u32 s23, s23, 0
	ds_read_b128 v[112:115], v240
	ds_read_b128 v[144:147], v240 offset:8192
	ds_read_b128 v[116:119], v241
	ds_read_b128 v[148:151], v241 offset:8192
	ds_read_b128 v[120:123], v242
	ds_read_b128 v[152:155], v242 offset:8192
	ds_read_b128 v[124:127], v243
	ds_read_b128 v[156:159], v243 offset:8192
	ds_read_b128 v[128:131], v240 offset:16384
	ds_read_b128 v[160:163], v240 offset:24576
	ds_read_b128 v[132:135], v241 offset:16384
	ds_read_b128 v[164:167], v241 offset:24576
	ds_read_b128 v[136:139], v242 offset:16384
	ds_read_b128 v[168:171], v242 offset:24576
	ds_read_b128 v[140:143], v243 offset:16384
	ds_read_b128 v[172:175], v243 offset:24576
	s_waitcnt vmcnt(2)
	s_waitcnt lgkmcnt(14)
	v_mfma_f32_16x16x32_f16 v[0:3], v[36:39], v[112:115], 0
	v_mfma_f32_16x16x32_f16 v[4:7], v[36:39], v[144:147], 0
	v_mfma_f32_16x16x32_f16 v[8:11], v[76:79], v[112:115], 0
	v_mfma_f32_16x16x32_f16 v[12:15], v[76:79], v[144:147], 0
	s_waitcnt lgkmcnt(12)
	v_mfma_f32_16x16x32_f16 v[0:3], v[32:35], v[116:119], v[0:3]
	v_mfma_f32_16x16x32_f16 v[4:7], v[32:35], v[148:151], v[4:7]
	v_mfma_f32_16x16x32_f16 v[8:11], v[72:75], v[116:119], v[8:11]
	v_mfma_f32_16x16x32_f16 v[12:15], v[72:75], v[148:151], v[12:15]
	s_waitcnt lgkmcnt(10)
	v_mfma_f32_16x16x32_f16 v[0:3], v[64:67], v[120:123], v[0:3]
	v_mfma_f32_16x16x32_f16 v[4:7], v[64:67], v[152:155], v[4:7]
	v_mfma_f32_16x16x32_f16 v[8:11], v[68:71], v[120:123], v[8:11]
	v_mfma_f32_16x16x32_f16 v[12:15], v[68:71], v[152:155], v[12:15]
	s_waitcnt lgkmcnt(8)
	v_mfma_f32_16x16x32_f16 v[0:3], v[48:51], v[124:127], v[0:3]
	v_mfma_f32_16x16x32_f16 v[4:7], v[48:51], v[156:159], v[4:7]
	v_mfma_f32_16x16x32_f16 v[8:11], v[52:55], v[124:127], v[8:11]
	v_mfma_f32_16x16x32_f16 v[12:15], v[52:55], v[156:159], v[12:15]
	s_waitcnt lgkmcnt(6)
	v_mfma_f32_16x16x32_f16 v[0:3], v[92:95], v[128:131], v[0:3]
	v_mfma_f32_16x16x32_f16 v[4:7], v[92:95], v[160:163], v[4:7]
	v_mfma_f32_16x16x32_f16 v[8:11], v[60:63], v[128:131], v[8:11]
	v_mfma_f32_16x16x32_f16 v[12:15], v[60:63], v[160:163], v[12:15]
	s_waitcnt lgkmcnt(4)
	v_mfma_f32_16x16x32_f16 v[0:3], v[84:87], v[132:135], v[0:3]
	v_mfma_f32_16x16x32_f16 v[4:7], v[84:87], v[164:167], v[4:7]
	v_mfma_f32_16x16x32_f16 v[8:11], v[56:59], v[132:135], v[8:11]
	v_mfma_f32_16x16x32_f16 v[12:15], v[56:59], v[164:167], v[12:15]
	s_waitcnt lgkmcnt(2)
	v_mfma_f32_16x16x32_f16 v[0:3], v[80:83], v[136:139], v[0:3]
	v_mfma_f32_16x16x32_f16 v[4:7], v[80:83], v[168:171], v[4:7]
	v_mfma_f32_16x16x32_f16 v[8:11], v[44:47], v[136:139], v[8:11]
	v_mfma_f32_16x16x32_f16 v[12:15], v[44:47], v[168:171], v[12:15]
	s_waitcnt lgkmcnt(0)
	v_mfma_f32_16x16x32_f16 v[0:3], v[88:91], v[140:143], v[0:3]
	v_mfma_f32_16x16x32_f16 v[4:7], v[88:91], v[172:175], v[4:7]
	v_mfma_f32_16x16x32_f16 v[8:11], v[40:43], v[140:143], v[8:11]
	v_mfma_f32_16x16x32_f16 v[12:15], v[40:43], v[172:175], v[12:15]
	ds_read_b128 v[176:179], v240 offset:4096
	ds_read_b128 v[208:211], v240 offset:12288
	ds_read_b128 v[180:183], v241 offset:4096
	ds_read_b128 v[212:215], v241 offset:12288
	ds_read_b128 v[184:187], v242 offset:4096
	ds_read_b128 v[216:219], v242 offset:12288
	ds_read_b128 v[188:191], v243 offset:4096
	ds_read_b128 v[220:223], v243 offset:12288
	ds_read_b128 v[192:195], v240 offset:20480
	ds_read_b128 v[224:227], v240 offset:28672
	ds_read_b128 v[196:199], v241 offset:20480
	ds_read_b128 v[228:231], v241 offset:28672
	ds_read_b128 v[200:203], v242 offset:20480
	ds_read_b128 v[232:235], v242 offset:28672
	ds_read_b128 v[204:207], v243 offset:20480
	ds_read_b128 v[236:239], v243 offset:28672
	s_waitcnt vmcnt(0)
	s_waitcnt lgkmcnt(14)
	v_mfma_f32_16x16x32_f16 v[16:19], v[36:39], v[176:179], 0
	v_mfma_f32_16x16x32_f16 v[20:23], v[36:39], v[208:211], 0
	v_mfma_f32_16x16x32_f16 v[24:27], v[76:79], v[176:179], 0
	v_mfma_f32_16x16x32_f16 v[28:31], v[76:79], v[208:211], 0
	s_add_u32 s26, s22, 0x0
	s_addc_u32 s27, s23, 0
	v_add_f32_e32 v104, v0, v96
	v_add_f32_e32 v105, v4, v96
	global_store_dwordx2 v244, v[104:105], s[26:27] nt
	s_waitcnt lgkmcnt(12)
	v_mfma_f32_16x16x32_f16 v[16:19], v[32:35], v[180:183], v[16:19]
	v_mfma_f32_16x16x32_f16 v[20:23], v[32:35], v[212:215], v[20:23]
	v_mfma_f32_16x16x32_f16 v[24:27], v[72:75], v[180:183], v[24:27]
	v_mfma_f32_16x16x32_f16 v[28:31], v[72:75], v[212:215], v[28:31]
	s_add_u32 s26, s22, 0x4000
	s_addc_u32 s27, s23, 0
	v_add_f32_e32 v106, v1, v97
	v_add_f32_e32 v107, v5, v97
	global_store_dwordx2 v244, v[106:107], s[26:27] nt
	s_waitcnt lgkmcnt(10)
	v_mfma_f32_16x16x32_f16 v[16:19], v[64:67], v[184:187], v[16:19]
	v_mfma_f32_16x16x32_f16 v[20:23], v[64:67], v[216:219], v[20:23]
	v_mfma_f32_16x16x32_f16 v[24:27], v[68:71], v[184:187], v[24:27]
	v_mfma_f32_16x16x32_f16 v[28:31], v[68:71], v[216:219], v[28:31]
	s_add_u32 s26, s22, 0x8000
	s_addc_u32 s27, s23, 0
	v_add_f32_e32 v108, v2, v98
	v_add_f32_e32 v109, v6, v98
	global_store_dwordx2 v244, v[108:109], s[26:27] nt
	s_waitcnt lgkmcnt(8)
	v_mfma_f32_16x16x32_f16 v[16:19], v[48:51], v[188:191], v[16:19]
	v_mfma_f32_16x16x32_f16 v[20:23], v[48:51], v[220:223], v[20:23]
	v_mfma_f32_16x16x32_f16 v[24:27], v[52:55], v[188:191], v[24:27]
	v_mfma_f32_16x16x32_f16 v[28:31], v[52:55], v[220:223], v[28:31]
	s_add_u32 s26, s22, 0xc000
	s_addc_u32 s27, s23, 0
	v_add_f32_e32 v110, v3, v99
	v_add_f32_e32 v111, v7, v99
	global_store_dwordx2 v244, v[110:111], s[26:27] nt
	s_waitcnt lgkmcnt(6)
	v_mfma_f32_16x16x32_f16 v[16:19], v[92:95], v[192:195], v[16:19]
	v_mfma_f32_16x16x32_f16 v[20:23], v[92:95], v[224:227], v[20:23]
	v_mfma_f32_16x16x32_f16 v[24:27], v[60:63], v[192:195], v[24:27]
	v_mfma_f32_16x16x32_f16 v[28:31], v[60:63], v[224:227], v[28:31]
	s_add_u32 s26, s22, 0x40000
	s_addc_u32 s27, s23, 0
	v_add_f32_e32 v104, v8, v100
	v_add_f32_e32 v105, v12, v100
	global_store_dwordx2 v244, v[104:105], s[26:27] nt
	s_waitcnt lgkmcnt(4)
	v_mfma_f32_16x16x32_f16 v[16:19], v[84:87], v[196:199], v[16:19]
	v_mfma_f32_16x16x32_f16 v[20:23], v[84:87], v[228:231], v[20:23]
	v_mfma_f32_16x16x32_f16 v[24:27], v[56:59], v[196:199], v[24:27]
	v_mfma_f32_16x16x32_f16 v[28:31], v[56:59], v[228:231], v[28:31]
	s_add_u32 s26, s22, 0x44000
	s_addc_u32 s27, s23, 0
	v_add_f32_e32 v106, v9, v101
	v_add_f32_e32 v107, v13, v101
	global_store_dwordx2 v244, v[106:107], s[26:27] nt
	s_waitcnt lgkmcnt(2)
	v_mfma_f32_16x16x32_f16 v[16:19], v[80:83], v[200:203], v[16:19]
	v_mfma_f32_16x16x32_f16 v[20:23], v[80:83], v[232:235], v[20:23]
	v_mfma_f32_16x16x32_f16 v[24:27], v[44:47], v[200:203], v[24:27]
	v_mfma_f32_16x16x32_f16 v[28:31], v[44:47], v[232:235], v[28:31]
	s_add_u32 s26, s22, 0x48000
	s_addc_u32 s27, s23, 0
	v_add_f32_e32 v108, v10, v102
	v_add_f32_e32 v109, v14, v102
	global_store_dwordx2 v244, v[108:109], s[26:27] nt
	s_waitcnt lgkmcnt(0)
	v_mfma_f32_16x16x32_f16 v[16:19], v[88:91], v[204:207], v[16:19]
	v_mfma_f32_16x16x32_f16 v[20:23], v[88:91], v[236:239], v[20:23]
	v_mfma_f32_16x16x32_f16 v[24:27], v[40:43], v[204:207], v[24:27]
	v_mfma_f32_16x16x32_f16 v[28:31], v[40:43], v[236:239], v[28:31]
	s_add_u32 s26, s22, 0x4c000
	s_addc_u32 s27, s23, 0
	v_add_f32_e32 v110, v11, v103
	v_add_f32_e32 v111, v15, v103
	global_store_dwordx2 v244, v[110:111], s[26:27] nt
	s_nop 7
	s_nop 1
	s_add_u32 s26, s22, 0x0
	s_addc_u32 s27, s23, 0
	v_add_f32_e32 v104, v16, v96
	v_add_f32_e32 v105, v20, v96
	global_store_dwordx2 v244, v[104:105], s[26:27] offset:128 nt
	s_add_u32 s26, s22, 0x4000
	s_addc_u32 s27, s23, 0
	v_add_f32_e32 v106, v17, v97
	v_add_f32_e32 v107, v21, v97
	global_store_dwordx2 v244, v[106:107], s[26:27] offset:128 nt
	s_add_u32 s26, s22, 0x8000
	s_addc_u32 s27, s23, 0
	v_add_f32_e32 v108, v18, v98
	v_add_f32_e32 v109, v22, v98
	global_store_dwordx2 v244, v[108:109], s[26:27] offset:128 nt
	s_add_u32 s26, s22, 0xc000
	s_addc_u32 s27, s23, 0
	v_add_f32_e32 v110, v19, v99
	v_add_f32_e32 v111, v23, v99
	global_store_dwordx2 v244, v[110:111], s[26:27] offset:128 nt
	s_add_u32 s26, s22, 0x40000
	s_addc_u32 s27, s23, 0
	v_add_f32_e32 v104, v24, v100
	v_add_f32_e32 v105, v28, v100
	global_store_dwordx2 v244, v[104:105], s[26:27] offset:128 nt
	s_add_u32 s26, s22, 0x44000
	s_addc_u32 s27, s23, 0
	v_add_f32_e32 v106, v25, v101
	v_add_f32_e32 v107, v29, v101
	global_store_dwordx2 v244, v[106:107], s[26:27] offset:128 nt
	s_add_u32 s26, s22, 0x48000
	s_addc_u32 s27, s23, 0
	v_add_f32_e32 v108, v26, v102
	v_add_f32_e32 v109, v30, v102
	global_store_dwordx2 v244, v[108:109], s[26:27] offset:128 nt
	s_add_u32 s26, s22, 0x4c000
	s_addc_u32 s27, s23, 0
	v_add_f32_e32 v110, v27, v103
	v_add_f32_e32 v111, v31, v103
	global_store_dwordx2 v244, v[110:111], s[26:27] offset:128 nt
	s_endpgm
